# prep: write-through (sc1) stores for the packed weight outputs so less dirty L2 data is left for the kernel boundary
# speedup vs baseline: 1.0031x; 1.0003x over previous
.LBB0_73:
	s_or_b64 exec, exec, s[8:9]
	v_mul_f32_e32 v1, 0x45800000, v19
	s_waitcnt vmcnt(2)
	v_mul_f32_e32 v2, 0x45800000, v20
	v_mul_f32_e32 v3, 0x45800000, v21
	s_waitcnt vmcnt(1)
	v_mul_f32_e32 v6, 0x45800000, v23
	v_mul_f32_e32 v4, 0x45800000, v24
	v_mul_f32_e32 v7, 0x45800000, v25
	v_mul_f32_e32 v5, 0x45800000, v10
	v_mul_f32_e32 v8, 0x45800000, v11
	v_ashrrev_i32_e32 v19, 31, v18
	v_cvt_pk_f16_f32 v5, v5, v8
	v_cvt_pk_f16_f32 v4, v4, v7
	v_cvt_pk_f16_f32 v3, v3, v6
	v_cvt_pk_f16_f32 v2, v1, v2
	v_lshl_add_u64 v[6:7], v[18:19], 4, s[6:7]
	global_store_dwordx4 v[6:7], v[2:5], off sc1

.LBB0_77:
	s_or_b64 exec, exec, s[0:1]
	s_and_b32 s10, s2, 3
	s_bfe_u32 s2, s2, 0x30002
	s_lshl_b32 s11, s2, 6
	s_lshl_b32 s0, s3, 20
	s_add_u32 s0, s4, s0
	s_addc_u32 s1, s5, 0
	s_lshl_b32 s4, s2, 17
	s_add_u32 s0, s0, s4
	s_addc_u32 s1, s1, 0
	s_lshl_b32 s4, s10, 9
	s_add_u32 s0, s0, s4
	s_addc_u32 s1, s1, 0
	s_waitcnt lgkmcnt(0)
	v_mov_b32_e32 v3, 0
	s_or_b32 s8, s11, s8
	v_lshrrev_b32_e32 v28, 5, v0
	v_or_b32_e32 v4, s8, v28
	v_mov_b32_e32 v5, v3
	v_lshl_add_u64 v[4:5], v[4:5], 2, s[16:17]
	s_barrier
	global_load_dword v29, v[4:5], off
	v_or_b32_e32 v14, 0x200, v0
	v_lshrrev_b32_e32 v33, 5, v14
	v_or_b32_e32 v2, 0x100, v0
	v_mov_b32_e32 v19, v3
	v_or_b32_e32 v18, s8, v33
	v_lshrrev_b32_e32 v30, 5, v2
	v_lshl_add_u64 v[18:19], v[18:19], 2, s[16:17]
	global_load_dword v34, v[18:19], off
	v_or_b32_e32 v4, s8, v30
	v_mov_b32_e32 v5, v3
	v_lshl_add_u64 v[4:5], v[4:5], 2, s[16:17]
	global_load_dword v31, v[4:5], off
	v_and_b32_e32 v20, 31, v0
	v_lshlrev_b32_e32 v2, 4, v20
	v_lshl_add_u64 v[4:5], s[0:1], 0, v[2:3]
	v_lshlrev_b32_e32 v2, 11, v28
	v_lshl_add_u64 v[6:7], v[4:5], 0, v[2:3]
	global_load_dwordx4 v[6:9], v[6:7], off
	v_mov_b32_e32 v15, v3
	v_lshlrev_b32_e32 v14, 11, v30
	v_lshl_add_u64 v[14:15], v[4:5], 0, v[14:15]
	global_load_dwordx4 v[14:17], v[14:15], off
	ds_read_b128 v[10:13], v3 offset:17408
	s_brev_b32 s11, 34
	v_or_b32_e32 v21, 0x300, v0
	v_lshrrev_b32_e32 v36, 5, v21
	v_mov_b32_e32 v19, v3
	s_waitcnt lgkmcnt(0)
	v_add_f32_e32 v10, v10, v11
	v_add_f32_e32 v10, v10, v12
	v_add_f32_e32 v37, v10, v13
	v_div_scale_f32 v38, s[0:1], v37, v37, s11
	v_rcp_f32_e32 v40, v38
	v_mov_b32_e32 v23, v3
	v_lshlrev_b32_e32 v18, 11, v33
	v_or_b32_e32 v22, s8, v36
	v_lshlrev_b32_e32 v35, 3, v20
	v_mov_b32_e32 v21, v3
	v_lshlrev_b32_e32 v20, 11, v36
	v_lshl_add_u64 v[24:25], v[4:5], 0, v[18:19]
	v_lshl_add_u64 v[22:23], v[22:23], 2, s[16:17]
	v_lshl_add_u64 v[26:27], v[4:5], 0, v[20:21]
	global_load_dwordx4 v[10:13], v[24:25], off
	global_load_dword v41, v[22:23], off
	global_load_dwordx4 v[18:21], v[26:27], off
	v_fma_f32 v22, -v38, v40, 1.0
	v_div_scale_f32 v39, vcc, s11, v37, s11
	v_fmac_f32_e32 v40, v22, v40
	v_mul_f32_e32 v22, v39, v40
	v_fma_f32 v23, -v38, v22, v39
	v_fmac_f32_e32 v22, v23, v40
	v_fma_f32 v23, -v38, v22, v39
	v_div_fmas_f32 v22, v23, v40, v22
	v_div_fixup_f32 v37, v22, v37, s11
	s_mov_b32 s5, 0x800000
	v_mov_b32_e32 v32, 0x42000000
	v_or_b32_e32 v2, 0x10000, v2
	s_mov_b32 s4, 0x39800000
	s_waitcnt vmcnt(7)
	v_mul_f32_e32 v22, v29, v29
	v_mul_f32_e32 v22, v37, v22
	v_max_f32_e32 v22, 0x2b8cbccc, v22
	v_cmp_gt_f32_e32 vcc, s5, v22
	s_waitcnt vmcnt(5)
	v_mul_f32_e32 v23, v31, v31
	v_cndmask_b32_e64 v24, 0, 32, vcc
	v_ldexp_f32 v22, v22, v24
	v_log_f32_e32 v22, v22
	v_mul_f32_e32 v23, v37, v23
	v_max_f32_e32 v23, 0x2b8cbccc, v23
	v_cndmask_b32_e32 v24, 0, v32, vcc
	v_cmp_gt_f32_e64 s[0:1], s5, v23
	v_sub_f32_e32 v22, v22, v24
	v_mul_f32_e32 v22, 0.5, v22
	v_cndmask_b32_e64 v25, 0, 32, s[0:1]
	v_ldexp_f32 v23, v23, v25
	v_rndne_f32_e32 v22, v22
	v_log_f32_e32 v25, v23
	v_cvt_i32_f32_e32 v24, v22
	v_lshl_add_u64 v[22:23], v[4:5], 0, v[2:3]
	v_cndmask_b32_e64 v2, 0, v32, s[0:1]
	v_sub_f32_e32 v25, v25, v2
	v_sub_u32_e32 v2, 0, v24
	v_med3_i32 v2, v2, -1, 3
	v_sub_u32_e32 v2, 0, v2
	v_ldexp_f32 v2, s4, v2
	s_waitcnt vmcnt(4)
	v_pk_mul_f32 v[6:7], v[6:7], v[2:3] op_sel_hi:[1,0]
	v_pk_mul_f32 v[8:9], v[8:9], v[2:3] op_sel_hi:[1,0]
	v_add_u32_e32 v2, s8, v28
	v_cvt_pk_f16_f32 v6, v6, v7
	v_cvt_pk_f16_f32 v7, v8, v9
	v_lshl_add_u64 v[8:9], v[2:3], 2, s[16:17]
	global_load_dword v29, v[8:9], off offset:128
	v_mul_f32_e32 v2, 0.5, v25
	v_rndne_f32_e32 v2, v2
	v_cvt_i32_f32_e32 v2, v2
	s_movk_i32 s0, 0x110
	v_mad_u32_u24 v28, v28, s0, v35
	ds_write_b64 v28, v[6:7]
	v_sub_u32_e32 v2, 0, v2
	v_med3_i32 v2, v2, -1, 3
	v_sub_u32_e32 v2, 0, v2
	v_ldexp_f32 v2, s4, v2
	s_waitcnt vmcnt(4)
	v_pk_mul_f32 v[6:7], v[14:15], v[2:3] op_sel_hi:[1,0]
	v_mul_f32_e32 v8, v34, v34
	v_cvt_pk_f16_f32 v14, v6, v7
	v_pk_mul_f32 v[6:7], v[16:17], v[2:3] op_sel_hi:[1,0]
	v_or_b32_e32 v2, 0x500, v0
	v_lshrrev_b32_e32 v31, 5, v2
	v_lshlrev_b32_e32 v2, 11, v31
	v_lshl_add_u64 v[16:17], v[4:5], 0, v[2:3]
	v_add_u32_e32 v2, s8, v31
	v_cvt_pk_f16_f32 v15, v6, v7
	v_lshl_add_u64 v[6:7], v[2:3], 2, s[16:17]
	v_mul_f32_e32 v2, v37, v8
	v_max_f32_e32 v2, 0x2b8cbccc, v2
	v_cmp_gt_f32_e32 vcc, s5, v2
	global_load_dword v34, v[6:7], off
	s_nop 0
	v_cndmask_b32_e64 v6, 0, 32, vcc
	v_ldexp_f32 v2, v2, v6
	v_log_f32_e32 v2, v2
	global_load_dwordx4 v[6:9], v[22:23], off
	v_mad_u32_u24 v22, v30, s0, v35
	ds_write_b64 v22, v[14:15]
	v_cndmask_b32_e32 v14, 0, v32, vcc
	v_sub_f32_e32 v2, v2, v14
	v_mul_f32_e32 v2, 0.5, v2
	v_rndne_f32_e32 v2, v2
	v_cvt_i32_f32_e32 v26, v2
	v_or_b32_e32 v2, 0x600, v0
	v_lshrrev_b32_e32 v30, 5, v2
	v_lshlrev_b32_e32 v2, 11, v30
	v_lshl_add_u64 v[22:23], v[4:5], 0, v[2:3]
	v_add_u32_e32 v2, s8, v30
	v_lshl_add_u64 v[24:25], v[2:3], 2, s[16:17]
	v_sub_u32_e32 v2, 0, v26
	v_med3_i32 v2, v2, -1, 3
	v_sub_u32_e32 v2, 0, v2
	global_load_dword v38, v[24:25], off
	v_ldexp_f32 v2, s4, v2
	s_waitcnt vmcnt(6)
	v_pk_mul_f32 v[10:11], v[10:11], v[2:3] op_sel_hi:[1,0]
	v_pk_mul_f32 v[26:27], v[12:13], v[2:3] op_sel_hi:[1,0]
	s_waitcnt vmcnt(5)
	v_mul_f32_e32 v2, v41, v41
	v_mul_f32_e32 v2, v37, v2
	v_max_f32_e32 v2, 0x2b8cbccc, v2
	v_cmp_gt_f32_e32 vcc, s5, v2
	v_cvt_pk_f16_f32 v24, v10, v11
	global_load_dwordx4 v[14:17], v[16:17], off
	v_cndmask_b32_e64 v10, 0, 32, vcc
	v_ldexp_f32 v2, v2, v10
	v_log_f32_e32 v25, v2
	v_or_b32_e32 v2, 0x700, v0
	v_lshrrev_b32_e32 v39, 5, v2
	v_lshlrev_b32_e32 v2, 11, v39
	v_lshl_add_u64 v[4:5], v[4:5], 0, v[2:3]
	v_add_u32_e32 v2, s8, v39
	global_load_dwordx4 v[10:13], v[22:23], off
	v_lshl_add_u64 v[22:23], v[2:3], 2, s[16:17]
	global_load_dword v40, v[22:23], off
	v_cndmask_b32_e32 v2, 0, v32, vcc
	v_sub_f32_e32 v2, v25, v2
	v_cvt_pk_f16_f32 v25, v26, v27
	v_mad_u32_u24 v22, v33, s0, v35
	ds_write_b64 v22, v[24:25]
	v_mul_f32_e32 v2, 0.5, v2
	v_rndne_f32_e32 v2, v2
	v_cvt_i32_f32_e32 v2, v2
	v_sub_u32_e32 v2, 0, v2
	s_waitcnt vmcnt(6)
	v_mul_f32_e32 v22, v29, v29
	v_mul_f32_e32 v22, v37, v22
	v_max_f32_e32 v22, 0x2b8cbccc, v22
	v_cmp_gt_f32_e32 vcc, s5, v22
	v_med3_i32 v2, v2, -1, 3
	v_sub_u32_e32 v2, 0, v2
	v_cndmask_b32_e64 v23, 0, 32, vcc
	v_ldexp_f32 v22, v22, v23
	v_log_f32_e32 v26, v22
	global_load_dwordx4 v[22:25], v[4:5], off
	v_ldexp_f32 v2, s4, v2
	v_pk_mul_f32 v[18:19], v[18:19], v[2:3] op_sel_hi:[1,0]
	s_nop 0
	v_cvt_pk_f16_f32 v4, v18, v19
	v_pk_mul_f32 v[18:19], v[20:21], v[2:3] op_sel_hi:[1,0]
	v_cndmask_b32_e32 v2, 0, v32, vcc
	v_sub_f32_e32 v2, v26, v2
	v_mul_f32_e32 v2, 0.5, v2
	v_rndne_f32_e32 v2, v2
	v_cvt_pk_f16_f32 v5, v18, v19
	v_mad_u32_u24 v18, v36, s0, v35
	v_cvt_i32_f32_e32 v2, v2
	ds_write_b64 v18, v[4:5]
	s_waitcnt vmcnt(6)
	v_mul_f32_e32 v4, v34, v34
	v_mul_f32_e32 v4, v37, v4
	v_max_f32_e32 v4, 0x2b8cbccc, v4
	v_cmp_gt_f32_e32 vcc, s5, v4
	v_sub_u32_e32 v2, 0, v2
	v_med3_i32 v2, v2, -1, 3
	v_cndmask_b32_e64 v5, 0, 32, vcc
	v_ldexp_f32 v4, v4, v5
	v_sub_u32_e32 v2, 0, v2
	v_log_f32_e32 v18, v4
	v_ldexp_f32 v2, s4, v2
	s_waitcnt vmcnt(5)
	v_pk_mul_f32 v[4:5], v[6:7], v[2:3] op_sel_hi:[1,0]
	v_pk_mul_f32 v[6:7], v[8:9], v[2:3] op_sel_hi:[1,0]
	v_cvt_pk_f16_f32 v4, v4, v5
	v_cndmask_b32_e32 v5, 0, v32, vcc
	v_sub_f32_e32 v5, v18, v5
	v_mul_f32_e32 v5, 0.5, v5
	v_rndne_f32_e32 v5, v5
	v_cvt_i32_f32_e32 v18, v5
	v_cvt_pk_f16_f32 v5, v6, v7
	ds_write_b64 v28, v[4:5] offset:8704
	s_waitcnt vmcnt(4)
	v_mul_f32_e32 v6, v38, v38
	v_mul_f32_e32 v6, v37, v6
	v_max_f32_e32 v6, 0x2b8cbccc, v6
	v_cmp_gt_f32_e32 vcc, s5, v6
	v_sub_u32_e32 v2, 0, v18
	v_med3_i32 v2, v2, -1, 3
	v_cndmask_b32_e64 v7, 0, 32, vcc
	v_ldexp_f32 v6, v6, v7
	v_log_f32_e32 v8, v6
	v_sub_u32_e32 v2, 0, v2
	v_ldexp_f32 v2, s4, v2
	s_waitcnt vmcnt(3)
	v_pk_mul_f32 v[4:5], v[14:15], v[2:3] op_sel_hi:[1,0]
	v_pk_mul_f32 v[6:7], v[16:17], v[2:3] op_sel_hi:[1,0]
	v_cndmask_b32_e32 v2, 0, v32, vcc
	v_sub_f32_e32 v2, v8, v2
	v_cvt_pk_f16_f32 v4, v4, v5
	v_mul_f32_e32 v2, 0.5, v2
	v_cvt_pk_f16_f32 v5, v6, v7
	v_mad_u32_u24 v6, v31, s0, v35
	v_rndne_f32_e32 v2, v2
	ds_write_b64 v6, v[4:5]
	s_waitcnt vmcnt(1)
	v_mul_f32_e32 v6, v40, v40
	v_cvt_i32_f32_e32 v2, v2
	v_mul_f32_e32 v6, v37, v6
	v_max_f32_e32 v6, 0x2b8cbccc, v6
	v_cmp_gt_f32_e32 vcc, s5, v6
	v_sub_u32_e32 v2, 0, v2
	v_med3_i32 v2, v2, -1, 3
	v_cndmask_b32_e64 v7, 0, 32, vcc
	v_ldexp_f32 v6, v6, v7
	v_log_f32_e32 v8, v6
	v_sub_u32_e32 v2, 0, v2
	v_ldexp_f32 v2, s4, v2
	v_pk_mul_f32 v[4:5], v[10:11], v[2:3] op_sel_hi:[1,0]
	v_pk_mul_f32 v[6:7], v[12:13], v[2:3] op_sel_hi:[1,0]
	v_cndmask_b32_e32 v2, 0, v32, vcc
	v_sub_f32_e32 v2, v8, v2
	v_mul_f32_e32 v2, 0.5, v2
	v_rndne_f32_e32 v2, v2
	v_cvt_i32_f32_e32 v2, v2
	v_cvt_pk_f16_f32 v4, v4, v5
	v_cvt_pk_f16_f32 v5, v6, v7
	v_mad_u32_u24 v6, v30, s0, v35
	v_sub_u32_e32 v2, 0, v2
	v_med3_i32 v2, v2, -1, 3
	v_sub_u32_e32 v2, 0, v2
	v_ldexp_f32 v2, s4, v2
	ds_write_b64 v6, v[4:5]
	s_waitcnt vmcnt(0)
	v_pk_mul_f32 v[4:5], v[22:23], v[2:3] op_sel_hi:[1,0]
	v_pk_mul_f32 v[6:7], v[24:25], v[2:3] op_sel_hi:[1,0]
	v_cvt_pk_f16_f32 v4, v4, v5
	v_cvt_pk_f16_f32 v5, v6, v7
	v_mad_u32_u24 v2, v39, s0, v35
	ds_write_b64 v2, v[4:5]
	v_lshrrev_b32_e32 v2, 6, v0
	v_and_b32_e32 v4, 15, v0
	v_lshl_or_b32 v4, v2, 4, v4
	v_and_b32_e32 v0, 48, v0
	v_lshrrev_b32_e32 v0, 1, v0
	v_mad_u32_u24 v12, v4, s0, v0
	s_lshl_b32 s0, s2, 12
	s_add_u32 s0, s6, s0
	s_addc_u32 s1, s7, 0
	v_lshlrev_b32_e32 v2, 10, v2
	v_lshl_add_u64 v[4:5], s[0:1], 0, v[2:3]
	v_lshlrev_b32_e32 v2, 4, v1
	s_waitcnt lgkmcnt(0)
	s_barrier
	v_lshl_add_u64 v[8:9], v[4:5], 0, v[2:3]
	ds_read_b64 v[0:1], v12
	ds_read_b64 v[2:3], v12 offset:32
	ds_read_b64 v[4:5], v12 offset:64
	ds_read_b64 v[6:7], v12 offset:96
	s_lshl_b32 s0, s3, 19
	s_lshl_b32 s1, s10, 17
	s_or_b32 s8, s0, s1
	v_lshl_add_u64 v[10:11], v[8:9], 0, s[8:9]
	s_or_b32 s0, s8, 0x8000
	s_mov_b32 s1, s9
	s_waitcnt lgkmcnt(2)
	global_store_dwordx4 v[10:11], v[0:3], off sc1
	s_nop 1
	v_lshl_add_u64 v[0:1], v[8:9], 0, s[0:1]
	s_waitcnt lgkmcnt(0)
	global_store_dwordx4 v[0:1], v[4:7], off sc1
	ds_read_b64 v[0:1], v12 offset:128
	ds_read_b64 v[2:3], v12 offset:160
	ds_read_b64 v[4:5], v12 offset:192
	ds_read_b64 v[6:7], v12 offset:224
	s_or_b32 s0, s8, 0x10000
	v_lshl_add_u64 v[10:11], v[8:9], 0, s[0:1]
	s_or_b32 s8, s8, 0x18000
	s_waitcnt lgkmcnt(2)
	global_store_dwordx4 v[10:11], v[0:3], off sc1
	s_nop 1
	v_lshl_add_u64 v[0:1], v[8:9], 0, s[8:9]
	s_waitcnt lgkmcnt(0)
	global_store_dwordx4 v[0:1], v[4:7], off sc1
	s_endpgm
